# F1 + post-barrier critical-path trim: rope-address VALU of the first half-trip moved behind the first eight fragment ds_reads
# speedup vs baseline: 1.0155x; 1.0100x over previous
.LBB0_757:
	ds_read_b128 v[64:67], v180 offset:49152
	ds_read_b128 v[68:71], v180 offset:57344
	ds_read_b128 v[200:203], v181 offset:49152
	ds_read_b128 v[226:229], v181 offset:57344
	ds_read_b128 v[230:233], v182 offset:49152
	ds_read_b128 v[234:237], v182 offset:57344
	ds_read_b128 v[238:241], v183 offset:49152
	ds_read_b128 v[242:245], v183 offset:57344
	s_add_i32 s6, 0, 0x12000
	v_add_u32_e32 v199, s6, v170
	v_add_u32_e32 v204, s6, v171
	v_add_u32_e32 v205, s6, v172
	s_waitcnt lgkmcnt(7)
	v_mfma_f32_32x32x16_bf16 v[80:95], v[64:67], v[124:127], 0
	s_add_i32 s12, s64, -1
	s_sub_i32 s80, s11, 64
	s_cmp_lt_u32 s12, 3
	s_cselect_b32 s80, s10, s80
	s_mul_i32 s81, s80, 0xc00
	s_add_i32 s85, s82, 0x8000
	s_mov_b32 m0, s85
	s_add_i32 s85, s82, 0x10000
	buffer_load_dwordx4 v154, s[72:75], s81 offen lds
	v_exp_f32_e32 v216, v128
	v_add_f32_e32 v128, 0, v222
	v_add_f32_e32 v128, v224, v128
	v_add_f32_e32 v128, v220, v128
	v_add_f32_e32 v128, v223, v128
	v_add_f32_e32 v128, v219, v128
	v_add_f32_e32 v128, v221, v128
	s_waitcnt lgkmcnt(6)
	v_mfma_f32_32x32x16_bf16 v[64:79], v[68:71], v[124:127], 0
	s_mov_b32 m0, s85
	s_add_i32 s85, s82, 0xa000
	buffer_load_dwordx4 v155, s[72:75], s81 offen lds
	v_add_f32_e32 v128, v217, v128
	v_add_f32_e32 v128, v218, v128
	v_add_f32_e32 v128, v212, v128
	v_add_f32_e32 v128, v214, v128
	v_add_f32_e32 v128, v211, v128
	v_add_f32_e32 v128, v213, v128
	v_exp_f32_e32 v138, v138
	s_waitcnt lgkmcnt(5)
	v_mfma_f32_32x32x16_bf16 v[80:95], v[200:203], v[120:123], v[80:95]
	s_mov_b32 m0, s85
	s_add_i32 s81, s81, 0x18000
	buffer_load_dwordx4 v154, s[72:75], s81 offen lds
	v_add_f32_e32 v128, v208, v128
	v_exp_f32_e32 v139, v139
	v_add_f32_e32 v128, v210, v128
	v_exp_f32_e32 v164, v136
	v_add_f32_e32 v128, v207, v128
	v_exp_f32_e32 v137, v137
	v_add_f32_e32 v128, v209, v128
	s_waitcnt lgkmcnt(4)
	v_mfma_f32_32x32x16_bf16 v[64:79], v[226:229], v[120:123], v[64:79]
	s_lshl_b32 s81, s83, 11
	s_add_i32 s85, s82, 0x4000
	s_mov_b32 m0, s85
	s_add_i32 s85, s82, 0x6000
	buffer_load_dwordx4 v158, s[76:79], s81 offen lds
	ds_read_b128 v[200:203], v184 offset:49152
	ds_read_b128 v[226:229], v184 offset:57344
	v_exp_f32_e32 v165, v132
	v_add_f32_e32 v128, v138, v128
	v_add_f32_e32 v128, v139, v128
	v_exp_f32_e32 v206, v130
	v_add_f32_e32 v128, v164, v128
	v_exp_f32_e32 v215, v131
	s_waitcnt lgkmcnt(5)
	v_mfma_f32_32x32x16_bf16 v[80:95], v[230:233], v[116:119], v[80:95]
	s_mov_b32 m0, s85
	s_add_i32 s81, s81, 0x10000
	buffer_load_dwordx4 v158, s[76:79], s81 offen lds
	s_mov_b32 s84, s80
	v_add_f32_e32 v128, v137, v128
	v_add_f32_e32 v128, v165, v128
	v_exp_f32_e32 v225, v129
	v_exp_f32_e32 v162, v162
	v_exp_f32_e32 v163, v163
	v_exp_f32_e32 v160, v160
	v_exp_f32_e32 v161, v161
	s_waitcnt lgkmcnt(4)
	v_mfma_f32_32x32x16_bf16 v[64:79], v[234:237], v[116:119], v[64:79]
	ds_read_b128 v[230:233], v185 offset:49152
	ds_read_b128 v[234:237], v185 offset:57344
	v_cvt_pk_bf16_f32 v129, v220, v223
	v_cvt_pk_bf16_f32 v130, v219, v221
	v_cvt_pk_bf16_f32 v131, v217, v218
	v_cvt_pk_bf16_f32 v132, v212, v214
	v_cvt_pk_bf16_f32 v136, v138, v139
	v_cvt_pk_bf16_f32 v137, v164, v137
	s_waitcnt lgkmcnt(5)
	v_mfma_f32_32x32x16_bf16 v[80:95], v[238:241], v[112:115], v[80:95]
	v_cvt_pk_bf16_f32 v139, v206, v215
	v_permlane32_swap_b32_e32 v129, v131
	s_nop 0
	v_permlane32_swap_b32_e32 v137, v139
	s_waitcnt lgkmcnt(4)
	v_mfma_f32_32x32x16_bf16 v[64:79], v[242:245], v[112:115], v[64:79]
	ds_read_b128 v[238:241], v186 offset:49152
	ds_read_b128 v[242:245], v186 offset:57344
	s_waitcnt lgkmcnt(5)
	v_mfma_f32_32x32x16_bf16 v[80:95], v[200:203], v[108:111], v[80:95]
	s_waitcnt lgkmcnt(4)
	v_mfma_f32_32x32x16_bf16 v[64:79], v[226:229], v[108:111], v[64:79]
	ds_read_b128 v[200:203], v187 offset:49152
	ds_read_b128 v[226:229], v187 offset:57344
	s_waitcnt lgkmcnt(5)
	v_mfma_f32_32x32x16_bf16 v[80:95], v[230:233], v[104:107], v[80:95]
	s_waitcnt lgkmcnt(4)
	v_mfma_f32_32x32x16_bf16 v[64:79], v[234:237], v[104:107], v[64:79]
	ds_read_b128 v[230:233], v199
	ds_read_b128 v[234:237], v199 offset:4096
	ds_read_b128 v[246:249], v190
	s_waitcnt lgkmcnt(6)
	v_mfma_f32_32x32x16_bf16 v[80:95], v[238:241], v[100:103], v[80:95]
	s_waitcnt lgkmcnt(5)
	v_mfma_f32_32x32x16_bf16 v[64:79], v[242:245], v[100:103], v[64:79]
	ds_read_b128 v[238:241], v204
	ds_read_b128 v[242:245], v204 offset:4096
	ds_read_b128 v[250:253], v190 offset:1024
	v_add_u32_e32 v204, s6, v173
	s_waitcnt lgkmcnt(7)
	v_mfma_f32_32x32x16_bf16 v[80:95], v[200:203], v[96:99], v[80:95]
	s_waitcnt lgkmcnt(6)
	v_mfma_f32_32x32x16_bf16 v[64:79], v[226:229], v[96:99], v[64:79]
	ds_read_b128 v[200:203], v205
	ds_read_b128 v[226:229], v205 offset:4096
	s_waitcnt lgkmcnt(5)
	v_mfma_f32_32x32x16_bf16 v[80:95], v[230:233], v[246:249], v[80:95]
	s_waitcnt lgkmcnt(5)
	v_mfma_f32_32x32x16_bf16 v[64:79], v[234:237], v[246:249], v[64:79]
	ds_read_b128 v[230:233], v204
	ds_read_b128 v[234:237], v204 offset:4096
	ds_read_b128 v[246:249], v190 offset:2048
	s_waitcnt lgkmcnt(5)
	v_mfma_f32_32x32x16_bf16 v[80:95], v[238:241], v[250:253], v[80:95]
	s_waitcnt lgkmcnt(5)
	v_mfma_f32_32x32x16_bf16 v[64:79], v[242:245], v[250:253], v[64:79]
	ds_read_b128 v[250:253], v190 offset:3072
	s_waitcnt lgkmcnt(1)
	v_mfma_f32_32x32x16_bf16 v[80:95], v[200:203], v[246:249], v[80:95]
	v_exp_f32_e32 v205, v133
	v_cvt_pk_bf16_f32 v133, v211, v213
	v_cvt_pk_bf16_f32 v138, v165, v205
	v_add_f32_e32 v128, v205, v128
	v_add_f32_e32 v128, v206, v128
	v_add_f32_e32 v128, v215, v128
	s_waitcnt lgkmcnt(1)
	v_mfma_f32_32x32x16_bf16 v[64:79], v[226:229], v[246:249], v[64:79]
	v_add_f32_e32 v128, v216, v128
	v_add_f32_e32 v128, v225, v128
	v_add_f32_e32 v128, v162, v128
	v_add_f32_e32 v128, v163, v128
	v_add_f32_e32 v128, v160, v128
	v_add_f32_e32 v128, v161, v128
	s_waitcnt lgkmcnt(0)
	v_mfma_f32_32x32x16_bf16 v[80:95], v[230:233], v[250:253], v[80:95]
	v_exp_f32_e32 v226, v134
	v_exp_f32_e32 v227, v135
	v_cvt_pk_bf16_f32 v134, v208, v210
	v_cvt_pk_bf16_f32 v135, v207, v209
	v_add_f32_e32 v128, v226, v128
	v_add_f32_e32 v203, v227, v128
	v_mov_b32_e32 v204, v203
	s_waitcnt lgkmcnt(0)
	v_mfma_f32_32x32x16_bf16 v[64:79], v[234:237], v[250:253], v[64:79]
	s_nop 0
	v_permlane32_swap_b32_e32 v203, v204
	v_cvt_pk_bf16_f32 v128, v222, v224
	v_cvt_pk_bf16_f32 v208, v216, v225
	v_cvt_pk_bf16_f32 v209, v162, v163
	v_cvt_pk_bf16_f32 v210, v160, v161
	v_cvt_pk_bf16_f32 v211, v226, v227
	v_permlane32_swap_b32_e32 v132, v134
	v_permlane32_swap_b32_e32 v128, v130
	v_permlane32_swap_b32_e32 v133, v135
	v_permlane32_swap_b32_e32 v136, v138
	v_permlane32_swap_b32_e32 v208, v210
	v_permlane32_swap_b32_e32 v209, v211
	ds_read_b64_tr_b16 v[160:161], v167 offset:0
	ds_read_b64_tr_b16 v[162:163], v167 offset:0x800
	ds_read_b64_tr_b16 v[232:233], v167 offset:0x1000
	ds_read_b64_tr_b16 v[234:235], v167 offset:0x1800
	ds_read_b64_tr_b16 v[236:237], v167 offset:0x2000
	ds_read_b64_tr_b16 v[238:239], v167 offset:0x2800
	ds_read_b64_tr_b16 v[240:241], v167 offset:0x3000
	ds_read_b64_tr_b16 v[242:243], v167 offset:0x3800
	v_max_f32_e32 v164, v81, v81
	v_max_f32_e32 v165, v80, v80
	v_max_f32_e32 v164, v165, v164
	v_max3_f32 v164, v164, v82, v83
	v_max3_f32 v164, v164, v84, v85
	v_max3_f32 v164, v164, v86, v87
	v_max3_f32 v164, v164, v88, v89
	v_max3_f32 v164, v164, v90, v91
	v_max3_f32 v164, v164, v92, v93
	v_max3_f32 v164, v164, v94, v95
	s_waitcnt lgkmcnt(0)
	v_mfma_f32_32x32x16_bf16 v[16:31], v[128:131], v[160:163], v[16:31]
	v_max3_f32 v160, v164, v64, v65
	v_max3_f32 v160, v160, v66, v67
	v_max3_f32 v160, v160, v68, v69
	v_mfma_f32_32x32x16_bf16 v[16:31], v[132:135], v[232:235], v[16:31]
	ds_read_b64_tr_b16 v[232:233], v167 offset:0x200
	ds_read_b64_tr_b16 v[234:235], v167 offset:0xa00
	v_max3_f32 v160, v160, v70, v71
	v_max3_f32 v160, v160, v72, v73
	v_max3_f32 v160, v160, v74, v75
	v_mfma_f32_32x32x16_bf16 v[16:31], v[136:139], v[236:239], v[16:31]
	ds_read_b64_tr_b16 v[236:237], v167 offset:0x1200
	ds_read_b64_tr_b16 v[238:239], v167 offset:0x1a00
	ds_read_b64_tr_b16 v[244:245], v167 offset:0x2200
	ds_read_b64_tr_b16 v[246:247], v167 offset:0x2a00
	ds_read_b64_tr_b16 v[248:249], v167 offset:0x3200
	ds_read_b64_tr_b16 v[250:251], v167 offset:0x3a00
	v_max3_f32 v160, v160, v76, v77
	v_max3_f32 v160, v160, v78, v79
	v_mov_b32_e32 v161, v160
	v_mfma_f32_32x32x16_bf16 v[16:31], v[208:211], v[240:243], v[16:31]
	v_max_f32_e32 v162, v198, v198
	v_permlane32_swap_b32_e32 v160, v161
	v_max_f32_e32 v161, v161, v161
	v_max_f32_e32 v160, v160, v160
	v_max_f32_e32 v160, v160, v161
	s_waitcnt lgkmcnt(0)
	v_mfma_f32_32x32x16_bf16 v[32:47], v[128:131], v[232:235], v[32:47]
	ds_read_b64_tr_b16 v[232:233], v167 offset:0x400
	ds_read_b64_tr_b16 v[234:235], v167 offset:0xc00
	v_sub_f32_e32 v161, v160, v198
	v_max_f32_e32 v160, v162, v160
	v_sub_f32_e32 v162, v198, v160
	v_mul_f32_e32 v162, 0x3dd53b94, v162
	v_exp_f32_e32 v162, v162
	v_mfma_f32_32x32x16_bf16 v[32:47], v[132:135], v[236:239], v[32:47]
	ds_read_b64_tr_b16 v[236:237], v167 offset:0x1400
	ds_read_b64_tr_b16 v[238:239], v167 offset:0x1c00
	ds_read_b64_tr_b16 v[240:241], v167 offset:0x2400
	ds_read_b64_tr_b16 v[242:243], v167 offset:0x2c00
	v_cmp_ge_f32_e32 vcc, s48, v161
	s_cmp_eq_u64 vcc, exec
	s_cselect_b64 s[6:7], -1, 0
	v_cndmask_b32_e64 v206, v162, 1.0, s[6:7]
	v_cndmask_b32_e64 v160, v160, v198, s[6:7]
	v_mul_f32_e32 v205, 0xbdd53b94, v160
	v_cmp_gt_f32_e32 vcc, 1.0, v206
	v_mfma_f32_32x32x16_bf16 v[32:47], v[136:139], v[244:247], v[32:47]
	ds_read_b64_tr_b16 v[244:245], v167 offset:0x3400
	ds_read_b64_tr_b16 v[246:247], v167 offset:0x3c00
	v_fmamk_f32 v87, v87, 0x3dd53b94, v205
	v_fmamk_f32 v80, v80, 0x3dd53b94, v205
	v_fmamk_f32 v81, v81, 0x3dd53b94, v205
	v_fmamk_f32 v82, v82, 0x3dd53b94, v205
	v_fmamk_f32 v83, v83, 0x3dd53b94, v205
	v_mfma_f32_32x32x16_bf16 v[32:47], v[208:211], v[248:251], v[32:47]
	v_fmamk_f32 v84, v84, 0x3dd53b94, v205
	v_fmamk_f32 v85, v85, 0x3dd53b94, v205
	v_fmamk_f32 v86, v86, 0x3dd53b94, v205
	v_fmamk_f32 v88, v88, 0x3dd53b94, v205
	v_fmamk_f32 v89, v89, 0x3dd53b94, v205
	s_waitcnt lgkmcnt(0)
	v_mfma_f32_32x32x16_bf16 v[0:15], v[128:131], v[232:235], v[0:15]
	ds_read_b64_tr_b16 v[232:233], v167 offset:0x600
	ds_read_b64_tr_b16 v[234:235], v167 offset:0xe00
	v_fmamk_f32 v90, v90, 0x3dd53b94, v205
	v_fmamk_f32 v91, v91, 0x3dd53b94, v205
	v_fmamk_f32 v92, v92, 0x3dd53b94, v205
	v_fmamk_f32 v93, v93, 0x3dd53b94, v205
	v_fmamk_f32 v94, v94, 0x3dd53b94, v205
	v_mfma_f32_32x32x16_bf16 v[0:15], v[132:135], v[236:239], v[0:15]
	ds_read_b64_tr_b16 v[236:237], v167 offset:0x1600
	ds_read_b64_tr_b16 v[238:239], v167 offset:0x1e00
	v_fmamk_f32 v95, v95, 0x3dd53b94, v205
	v_fmamk_f32 v215, v64, 0x3dd53b94, v205
	v_fmamk_f32 v216, v65, 0x3dd53b94, v205
	v_fmamk_f32 v217, v66, 0x3dd53b94, v205
	v_fmamk_f32 v218, v67, 0x3dd53b94, v205
	v_mfma_f32_32x32x16_bf16 v[0:15], v[136:139], v[240:243], v[0:15]
	ds_read_b64_tr_b16 v[240:241], v167 offset:0x2600
	ds_read_b64_tr_b16 v[242:243], v167 offset:0x2e00
	ds_read_b64_tr_b16 v[248:249], v167 offset:0x3600
	ds_read_b64_tr_b16 v[250:251], v167 offset:0x3e00
	v_fmamk_f32 v219, v68, 0x3dd53b94, v205
	v_fmamk_f32 v212, v73, 0x3dd53b94, v205
	v_fmamk_f32 v213, v74, 0x3dd53b94, v205
	v_fmamk_f32 v214, v75, 0x3dd53b94, v205
	v_mfma_f32_32x32x16_bf16 v[0:15], v[208:211], v[244:247], v[0:15]
	v_fmamk_f32 v207, v76, 0x3dd53b94, v205
	v_fmamk_f32 v220, v77, 0x3dd53b94, v205
	v_fmamk_f32 v221, v78, 0x3dd53b94, v205
	s_waitcnt lgkmcnt(0)
	v_mfma_f32_32x32x16_bf16 v[48:63], v[128:131], v[232:235], v[48:63]
	v_exp_f32_e32 v128, v80
	v_exp_f32_e32 v129, v82
	v_exp_f32_e32 v130, v84
	v_exp_f32_e32 v131, v86
	v_mfma_f32_32x32x16_bf16 v[48:63], v[132:135], v[236:239], v[48:63]
	v_exp_f32_e32 v132, v88
	v_exp_f32_e32 v133, v90
	v_exp_f32_e32 v134, v92
	v_exp_f32_e32 v135, v94
	v_mfma_f32_32x32x16_bf16 v[48:63], v[136:139], v[240:243], v[48:63]
	v_exp_f32_e32 v139, v89
	v_exp_f32_e32 v138, v91
	v_exp_f32_e32 v137, v93
	v_exp_f32_e32 v136, v95
	v_mfma_f32_32x32x16_bf16 v[48:63], v[208:211], v[248:251], v[48:63]
	v_exp_f32_e32 v161, v87
	v_exp_f32_e32 v198, v81
	v_exp_f32_e32 v163, v83
	v_exp_f32_e32 v162, v85
	v_fmamk_f32 v208, v69, 0x3dd53b94, v205
	v_fmamk_f32 v209, v70, 0x3dd53b94, v205
	v_fmamk_f32 v210, v71, 0x3dd53b94, v205
	v_fmamk_f32 v211, v72, 0x3dd53b94, v205
	v_fmac_f32_e32 v205, 0x3dd53b94, v79
	s_cbranch_vccz .LBB0_761
	s_and_saveexec_b64 s[8:9], s[4:5]
	ds_write_b32 v189, v206 offset:128
	s_or_b64 exec, exec, s[8:9]
	s_waitcnt lgkmcnt(0)
	v_add_u32_e32 v248, s62, v169
	ds_read_b128 v[232:235], v248 offset:224
	ds_read_b128 v[236:239], v248 offset:192
	ds_read_b128 v[240:243], v248 offset:160
	ds_read_b128 v[244:247], v248 offset:128
	s_waitcnt lgkmcnt(3)
	v_pk_mul_f32 v[28:29], v[28:29], v[232:233]
	s_waitcnt lgkmcnt(2)
	v_pk_mul_f32 v[24:25], v[24:25], v[236:237]
	s_waitcnt lgkmcnt(1)
	v_pk_mul_f32 v[20:21], v[20:21], v[240:241]
	v_pk_mul_f32 v[30:31], v[30:31], v[234:235]
	v_pk_mul_f32 v[26:27], v[26:27], v[238:239]
	v_pk_mul_f32 v[22:23], v[22:23], v[242:243]
	s_waitcnt lgkmcnt(0)
	v_pk_mul_f32 v[18:19], v[18:19], v[246:247]
	v_pk_mul_f32 v[16:17], v[16:17], v[244:245]
	v_pk_mul_f32 v[44:45], v[44:45], v[232:233]
	v_pk_mul_f32 v[40:41], v[40:41], v[236:237]
	v_pk_mul_f32 v[36:37], v[36:37], v[240:241]
	v_pk_mul_f32 v[46:47], v[46:47], v[234:235]
	v_pk_mul_f32 v[42:43], v[42:43], v[238:239]
	v_pk_mul_f32 v[38:39], v[38:39], v[242:243]
	v_pk_mul_f32 v[34:35], v[34:35], v[246:247]
	v_pk_mul_f32 v[32:33], v[32:33], v[244:245]
	v_pk_mul_f32 v[12:13], v[12:13], v[232:233]
	v_pk_mul_f32 v[8:9], v[8:9], v[236:237]
	v_pk_mul_f32 v[4:5], v[4:5], v[240:241]
	v_pk_mul_f32 v[14:15], v[14:15], v[234:235]
	v_pk_mul_f32 v[10:11], v[10:11], v[238:239]
	v_pk_mul_f32 v[6:7], v[6:7], v[242:243]
	v_pk_mul_f32 v[2:3], v[2:3], v[246:247]
	v_pk_mul_f32 v[0:1], v[0:1], v[244:245]
	v_pk_mul_f32 v[60:61], v[60:61], v[232:233]
	v_pk_mul_f32 v[56:57], v[56:57], v[236:237]
	v_pk_mul_f32 v[52:53], v[52:53], v[240:241]
	v_pk_mul_f32 v[62:63], v[62:63], v[234:235]
	v_pk_mul_f32 v[58:59], v[58:59], v[238:239]
	v_pk_mul_f32 v[54:55], v[54:55], v[242:243]
	v_pk_mul_f32 v[50:51], v[50:51], v[246:247]
	v_pk_mul_f32 v[48:49], v[48:49], v[244:245]

.LBB0_2012:
	ds_read_b128 v[64:67], v180 offset:49152
	ds_read_b128 v[68:71], v180 offset:57344
	ds_read_b128 v[200:203], v181 offset:49152
	ds_read_b128 v[226:229], v181 offset:57344
	ds_read_b128 v[230:233], v182 offset:49152
	ds_read_b128 v[234:237], v182 offset:57344
	ds_read_b128 v[238:241], v183 offset:49152
	ds_read_b128 v[242:245], v183 offset:57344
	s_add_i32 s6, 0, 0x12000
	v_add_u32_e32 v199, s6, v170
	v_add_u32_e32 v204, s6, v171
	v_add_u32_e32 v205, s6, v172
	s_waitcnt lgkmcnt(7)
	v_mfma_f32_32x32x16_bf16 v[80:95], v[64:67], v[124:127], 0
	s_add_i32 s8, s8, 2
	s_sub_i32 s80, s14, 64
	s_cmp_lt_u32 s8, 3
	s_cselect_b32 s80, s13, s80
	s_mul_i32 s81, s80, 0xc00
	s_add_i32 s85, s82, 0x8000
	s_mov_b32 m0, s85
	s_add_i32 s85, s82, 0x10000
	buffer_load_dwordx4 v154, s[72:75], s81 offen lds
	v_exp_f32_e32 v216, v128
	v_add_f32_e32 v128, 0, v222
	v_add_f32_e32 v128, v224, v128
	v_add_f32_e32 v128, v220, v128
	v_add_f32_e32 v128, v223, v128
	v_add_f32_e32 v128, v219, v128
	v_add_f32_e32 v128, v221, v128
	s_waitcnt lgkmcnt(6)
	v_mfma_f32_32x32x16_bf16 v[64:79], v[68:71], v[124:127], 0
	s_mov_b32 m0, s85
	s_add_i32 s85, s82, 0xa000
	buffer_load_dwordx4 v155, s[72:75], s81 offen lds
	v_add_f32_e32 v128, v217, v128
	v_add_f32_e32 v128, v218, v128
	v_add_f32_e32 v128, v212, v128
	v_add_f32_e32 v128, v214, v128
	v_add_f32_e32 v128, v211, v128
	v_add_f32_e32 v128, v213, v128
	v_exp_f32_e32 v138, v138
	s_waitcnt lgkmcnt(5)
	v_mfma_f32_32x32x16_bf16 v[80:95], v[200:203], v[120:123], v[80:95]
	s_mov_b32 m0, s85
	s_add_i32 s81, s81, 0x18000
	buffer_load_dwordx4 v154, s[72:75], s81 offen lds
	v_add_f32_e32 v128, v208, v128
	v_exp_f32_e32 v139, v139
	v_add_f32_e32 v128, v210, v128
	v_exp_f32_e32 v164, v136
	v_add_f32_e32 v128, v207, v128
	v_exp_f32_e32 v137, v137
	v_add_f32_e32 v128, v209, v128
	s_waitcnt lgkmcnt(4)
	v_mfma_f32_32x32x16_bf16 v[64:79], v[226:229], v[120:123], v[64:79]
	s_lshl_b32 s81, s83, 11
	s_add_i32 s85, s82, 0x4000
	s_mov_b32 m0, s85
	s_add_i32 s85, s82, 0x6000
	buffer_load_dwordx4 v158, s[76:79], s81 offen lds
	ds_read_b128 v[200:203], v184 offset:49152
	ds_read_b128 v[226:229], v184 offset:57344
	v_exp_f32_e32 v165, v132
	v_add_f32_e32 v128, v138, v128
	v_add_f32_e32 v128, v139, v128
	v_exp_f32_e32 v206, v130
	v_add_f32_e32 v128, v164, v128
	v_exp_f32_e32 v215, v131
	s_waitcnt lgkmcnt(5)
	v_mfma_f32_32x32x16_bf16 v[80:95], v[230:233], v[116:119], v[80:95]
	s_mov_b32 m0, s85
	s_add_i32 s81, s81, 0x10000
	buffer_load_dwordx4 v158, s[76:79], s81 offen lds
	s_mov_b32 s84, s80
	v_add_f32_e32 v128, v137, v128
	v_add_f32_e32 v128, v165, v128
	v_exp_f32_e32 v225, v129
	v_exp_f32_e32 v162, v162
	v_exp_f32_e32 v163, v163
	v_exp_f32_e32 v160, v160
	v_exp_f32_e32 v161, v161
	s_waitcnt lgkmcnt(4)
	v_mfma_f32_32x32x16_bf16 v[64:79], v[234:237], v[116:119], v[64:79]
	ds_read_b128 v[230:233], v185 offset:49152
	ds_read_b128 v[234:237], v185 offset:57344
	v_cvt_pk_bf16_f32 v129, v220, v223
	v_cvt_pk_bf16_f32 v130, v219, v221
	v_cvt_pk_bf16_f32 v131, v217, v218
	v_cvt_pk_bf16_f32 v132, v212, v214
	v_cvt_pk_bf16_f32 v136, v138, v139
	v_cvt_pk_bf16_f32 v137, v164, v137
	s_waitcnt lgkmcnt(5)
	v_mfma_f32_32x32x16_bf16 v[80:95], v[238:241], v[112:115], v[80:95]
	v_cvt_pk_bf16_f32 v139, v206, v215
	v_permlane32_swap_b32_e32 v129, v131
	s_nop 0
	v_permlane32_swap_b32_e32 v137, v139
	s_waitcnt lgkmcnt(4)
	v_mfma_f32_32x32x16_bf16 v[64:79], v[242:245], v[112:115], v[64:79]
	ds_read_b128 v[238:241], v186 offset:49152
	ds_read_b128 v[242:245], v186 offset:57344
	s_waitcnt lgkmcnt(5)
	v_mfma_f32_32x32x16_bf16 v[80:95], v[200:203], v[108:111], v[80:95]
	s_waitcnt lgkmcnt(4)
	v_mfma_f32_32x32x16_bf16 v[64:79], v[226:229], v[108:111], v[64:79]
	ds_read_b128 v[200:203], v187 offset:49152
	ds_read_b128 v[226:229], v187 offset:57344
	s_waitcnt lgkmcnt(5)
	v_mfma_f32_32x32x16_bf16 v[80:95], v[230:233], v[104:107], v[80:95]
	s_waitcnt lgkmcnt(4)
	v_mfma_f32_32x32x16_bf16 v[64:79], v[234:237], v[104:107], v[64:79]
	ds_read_b128 v[230:233], v199
	ds_read_b128 v[234:237], v199 offset:4096
	ds_read_b128 v[246:249], v190
	s_waitcnt lgkmcnt(6)
	v_mfma_f32_32x32x16_bf16 v[80:95], v[238:241], v[100:103], v[80:95]
	s_waitcnt lgkmcnt(5)
	v_mfma_f32_32x32x16_bf16 v[64:79], v[242:245], v[100:103], v[64:79]
	ds_read_b128 v[238:241], v204
	ds_read_b128 v[242:245], v204 offset:4096
	ds_read_b128 v[250:253], v190 offset:1024
	v_add_u32_e32 v204, s6, v173
	s_waitcnt lgkmcnt(7)
	v_mfma_f32_32x32x16_bf16 v[80:95], v[200:203], v[96:99], v[80:95]
	s_waitcnt lgkmcnt(6)
	v_mfma_f32_32x32x16_bf16 v[64:79], v[226:229], v[96:99], v[64:79]
	ds_read_b128 v[200:203], v205
	ds_read_b128 v[226:229], v205 offset:4096
	s_waitcnt lgkmcnt(5)
	v_mfma_f32_32x32x16_bf16 v[80:95], v[230:233], v[246:249], v[80:95]
	s_waitcnt lgkmcnt(5)
	v_mfma_f32_32x32x16_bf16 v[64:79], v[234:237], v[246:249], v[64:79]
	ds_read_b128 v[230:233], v204
	ds_read_b128 v[234:237], v204 offset:4096
	ds_read_b128 v[246:249], v190 offset:2048
	s_waitcnt lgkmcnt(5)
	v_mfma_f32_32x32x16_bf16 v[80:95], v[238:241], v[250:253], v[80:95]
	s_waitcnt lgkmcnt(5)
	v_mfma_f32_32x32x16_bf16 v[64:79], v[242:245], v[250:253], v[64:79]
	ds_read_b128 v[250:253], v190 offset:3072
	s_waitcnt lgkmcnt(1)
	v_mfma_f32_32x32x16_bf16 v[80:95], v[200:203], v[246:249], v[80:95]
	v_exp_f32_e32 v205, v133
	v_cvt_pk_bf16_f32 v133, v211, v213
	v_cvt_pk_bf16_f32 v138, v165, v205
	v_add_f32_e32 v128, v205, v128
	v_add_f32_e32 v128, v206, v128
	v_add_f32_e32 v128, v215, v128
	s_waitcnt lgkmcnt(1)
	v_mfma_f32_32x32x16_bf16 v[64:79], v[226:229], v[246:249], v[64:79]
	v_add_f32_e32 v128, v216, v128
	v_add_f32_e32 v128, v225, v128
	v_add_f32_e32 v128, v162, v128
	v_add_f32_e32 v128, v163, v128
	v_add_f32_e32 v128, v160, v128
	v_add_f32_e32 v128, v161, v128
	s_waitcnt lgkmcnt(0)
	v_mfma_f32_32x32x16_bf16 v[80:95], v[230:233], v[250:253], v[80:95]
	v_exp_f32_e32 v226, v134
	v_exp_f32_e32 v227, v135
	v_cvt_pk_bf16_f32 v134, v208, v210
	v_cvt_pk_bf16_f32 v135, v207, v209
	v_add_f32_e32 v128, v226, v128
	v_add_f32_e32 v203, v227, v128
	v_mov_b32_e32 v204, v203
	s_waitcnt lgkmcnt(0)
	v_mfma_f32_32x32x16_bf16 v[64:79], v[234:237], v[250:253], v[64:79]
	s_nop 0
	v_permlane32_swap_b32_e32 v203, v204
	v_cvt_pk_bf16_f32 v128, v222, v224
	v_cvt_pk_bf16_f32 v208, v216, v225
	v_cvt_pk_bf16_f32 v209, v162, v163
	v_cvt_pk_bf16_f32 v210, v160, v161
	v_cvt_pk_bf16_f32 v211, v226, v227
	v_permlane32_swap_b32_e32 v132, v134
	v_permlane32_swap_b32_e32 v128, v130
	v_permlane32_swap_b32_e32 v133, v135
	v_permlane32_swap_b32_e32 v136, v138
	v_permlane32_swap_b32_e32 v208, v210
	v_permlane32_swap_b32_e32 v209, v211
	ds_read_b64_tr_b16 v[160:161], v167 offset:0
	ds_read_b64_tr_b16 v[162:163], v167 offset:0x800
	ds_read_b64_tr_b16 v[232:233], v167 offset:0x1000
	ds_read_b64_tr_b16 v[234:235], v167 offset:0x1800
	ds_read_b64_tr_b16 v[236:237], v167 offset:0x2000
	ds_read_b64_tr_b16 v[238:239], v167 offset:0x2800
	ds_read_b64_tr_b16 v[240:241], v167 offset:0x3000
	ds_read_b64_tr_b16 v[242:243], v167 offset:0x3800
	v_max_f32_e32 v164, v81, v81
	v_max_f32_e32 v165, v80, v80
	v_max_f32_e32 v164, v165, v164
	v_max3_f32 v164, v164, v82, v83
	v_max3_f32 v164, v164, v84, v85
	v_max3_f32 v164, v164, v86, v87
	v_max3_f32 v164, v164, v88, v89
	v_max3_f32 v164, v164, v90, v91
	v_max3_f32 v164, v164, v92, v93
	v_max3_f32 v164, v164, v94, v95
	s_waitcnt lgkmcnt(0)
	v_mfma_f32_32x32x16_bf16 v[0:15], v[128:131], v[160:163], v[0:15]
	v_max3_f32 v160, v164, v64, v65
	v_max3_f32 v160, v160, v66, v67
	v_max3_f32 v160, v160, v68, v69
	v_mfma_f32_32x32x16_bf16 v[0:15], v[132:135], v[232:235], v[0:15]
	ds_read_b64_tr_b16 v[232:233], v167 offset:0x200
	ds_read_b64_tr_b16 v[234:235], v167 offset:0xa00
	v_max3_f32 v160, v160, v70, v71
	v_max3_f32 v160, v160, v72, v73
	v_max3_f32 v160, v160, v74, v75
	v_mfma_f32_32x32x16_bf16 v[0:15], v[136:139], v[236:239], v[0:15]
	ds_read_b64_tr_b16 v[236:237], v167 offset:0x1200
	ds_read_b64_tr_b16 v[238:239], v167 offset:0x1a00
	ds_read_b64_tr_b16 v[244:245], v167 offset:0x2200
	ds_read_b64_tr_b16 v[246:247], v167 offset:0x2a00
	ds_read_b64_tr_b16 v[248:249], v167 offset:0x3200
	ds_read_b64_tr_b16 v[250:251], v167 offset:0x3a00
	v_max3_f32 v160, v160, v76, v77
	v_max3_f32 v160, v160, v78, v79
	v_mov_b32_e32 v161, v160
	v_mfma_f32_32x32x16_bf16 v[0:15], v[208:211], v[240:243], v[0:15]
	v_max_f32_e32 v162, v198, v198
	v_permlane32_swap_b32_e32 v160, v161
	v_max_f32_e32 v161, v161, v161
	v_max_f32_e32 v160, v160, v160
	v_max_f32_e32 v160, v160, v161
	s_waitcnt lgkmcnt(0)
	v_mfma_f32_32x32x16_bf16 v[32:47], v[128:131], v[232:235], v[32:47]
	ds_read_b64_tr_b16 v[232:233], v167 offset:0x400
	ds_read_b64_tr_b16 v[234:235], v167 offset:0xc00
	v_sub_f32_e32 v161, v160, v198
	v_max_f32_e32 v160, v162, v160
	v_sub_f32_e32 v162, v198, v160
	v_mul_f32_e32 v162, 0x3dd53b94, v162
	v_exp_f32_e32 v162, v162
	v_mfma_f32_32x32x16_bf16 v[32:47], v[132:135], v[236:239], v[32:47]
	ds_read_b64_tr_b16 v[236:237], v167 offset:0x1400
	ds_read_b64_tr_b16 v[238:239], v167 offset:0x1c00
	ds_read_b64_tr_b16 v[240:241], v167 offset:0x2400
	ds_read_b64_tr_b16 v[242:243], v167 offset:0x2c00
	v_cmp_ge_f32_e32 vcc, s46, v161
	s_cmp_eq_u64 vcc, exec
	s_cselect_b64 s[6:7], -1, 0
	v_cndmask_b32_e64 v206, v162, 1.0, s[6:7]
	v_cndmask_b32_e64 v160, v160, v198, s[6:7]
	v_mul_f32_e32 v205, 0xbdd53b94, v160
	v_cmp_gt_f32_e32 vcc, 1.0, v206
	v_mfma_f32_32x32x16_bf16 v[32:47], v[136:139], v[244:247], v[32:47]
	ds_read_b64_tr_b16 v[244:245], v167 offset:0x3400
	ds_read_b64_tr_b16 v[246:247], v167 offset:0x3c00
	v_fmamk_f32 v87, v87, 0x3dd53b94, v205
	v_fmamk_f32 v80, v80, 0x3dd53b94, v205
	v_fmamk_f32 v81, v81, 0x3dd53b94, v205
	v_fmamk_f32 v82, v82, 0x3dd53b94, v205
	v_fmamk_f32 v83, v83, 0x3dd53b94, v205
	v_mfma_f32_32x32x16_bf16 v[32:47], v[208:211], v[248:251], v[32:47]
	v_fmamk_f32 v84, v84, 0x3dd53b94, v205
	v_fmamk_f32 v85, v85, 0x3dd53b94, v205
	v_fmamk_f32 v86, v86, 0x3dd53b94, v205
	v_fmamk_f32 v88, v88, 0x3dd53b94, v205
	v_fmamk_f32 v89, v89, 0x3dd53b94, v205
	s_waitcnt lgkmcnt(0)
	v_mfma_f32_32x32x16_bf16 v[16:31], v[128:131], v[232:235], v[16:31]
	ds_read_b64_tr_b16 v[232:233], v167 offset:0x600
	ds_read_b64_tr_b16 v[234:235], v167 offset:0xe00
	v_fmamk_f32 v90, v90, 0x3dd53b94, v205
	v_fmamk_f32 v91, v91, 0x3dd53b94, v205
	v_fmamk_f32 v92, v92, 0x3dd53b94, v205
	v_fmamk_f32 v93, v93, 0x3dd53b94, v205
	v_fmamk_f32 v94, v94, 0x3dd53b94, v205
	v_mfma_f32_32x32x16_bf16 v[16:31], v[132:135], v[236:239], v[16:31]
	ds_read_b64_tr_b16 v[236:237], v167 offset:0x1600
	ds_read_b64_tr_b16 v[238:239], v167 offset:0x1e00
	v_fmamk_f32 v95, v95, 0x3dd53b94, v205
	v_fmamk_f32 v215, v64, 0x3dd53b94, v205
	v_fmamk_f32 v216, v65, 0x3dd53b94, v205
	v_fmamk_f32 v217, v66, 0x3dd53b94, v205
	v_fmamk_f32 v218, v67, 0x3dd53b94, v205
	v_mfma_f32_32x32x16_bf16 v[16:31], v[136:139], v[240:243], v[16:31]
	ds_read_b64_tr_b16 v[240:241], v167 offset:0x2600
	ds_read_b64_tr_b16 v[242:243], v167 offset:0x2e00
	ds_read_b64_tr_b16 v[248:249], v167 offset:0x3600
	ds_read_b64_tr_b16 v[250:251], v167 offset:0x3e00
	v_fmamk_f32 v219, v68, 0x3dd53b94, v205
	v_fmamk_f32 v212, v73, 0x3dd53b94, v205
	v_fmamk_f32 v213, v74, 0x3dd53b94, v205
	v_fmamk_f32 v214, v75, 0x3dd53b94, v205
	v_mfma_f32_32x32x16_bf16 v[16:31], v[208:211], v[244:247], v[16:31]
	v_fmamk_f32 v207, v76, 0x3dd53b94, v205
	v_fmamk_f32 v220, v77, 0x3dd53b94, v205
	v_fmamk_f32 v221, v78, 0x3dd53b94, v205
	s_waitcnt lgkmcnt(0)
	v_mfma_f32_32x32x16_bf16 v[48:63], v[128:131], v[232:235], v[48:63]
	v_exp_f32_e32 v128, v80
	v_exp_f32_e32 v129, v82
	v_exp_f32_e32 v130, v84
	v_exp_f32_e32 v131, v86
	v_mfma_f32_32x32x16_bf16 v[48:63], v[132:135], v[236:239], v[48:63]
	v_exp_f32_e32 v132, v88
	v_exp_f32_e32 v133, v90
	v_exp_f32_e32 v134, v92
	v_exp_f32_e32 v135, v94
	v_mfma_f32_32x32x16_bf16 v[48:63], v[136:139], v[240:243], v[48:63]
	v_exp_f32_e32 v139, v89
	v_exp_f32_e32 v138, v91
	v_exp_f32_e32 v137, v93
	v_exp_f32_e32 v136, v95
	v_mfma_f32_32x32x16_bf16 v[48:63], v[208:211], v[248:251], v[48:63]
	v_exp_f32_e32 v161, v87
	v_exp_f32_e32 v198, v81
	v_exp_f32_e32 v163, v83
	v_exp_f32_e32 v162, v85
	v_fmamk_f32 v208, v69, 0x3dd53b94, v205
	v_fmamk_f32 v209, v70, 0x3dd53b94, v205
	v_fmamk_f32 v210, v71, 0x3dd53b94, v205
	v_fmamk_f32 v211, v72, 0x3dd53b94, v205
	v_fmac_f32_e32 v205, 0x3dd53b94, v79
	s_cbranch_vccz .LBB0_2016
	s_and_saveexec_b64 s[10:11], s[4:5]
	ds_write_b32 v189, v206 offset:128
	s_or_b64 exec, exec, s[10:11]
	s_waitcnt lgkmcnt(0)
	v_add_u32_e32 v248, s12, v169
	ds_read_b128 v[232:235], v248 offset:224
	ds_read_b128 v[236:239], v248 offset:192
	ds_read_b128 v[240:243], v248 offset:160
	ds_read_b128 v[244:247], v248 offset:128
	s_waitcnt lgkmcnt(3)
	v_pk_mul_f32 v[12:13], v[12:13], v[232:233]
	s_waitcnt lgkmcnt(2)
	v_pk_mul_f32 v[8:9], v[8:9], v[236:237]
	s_waitcnt lgkmcnt(1)
	v_pk_mul_f32 v[4:5], v[4:5], v[240:241]
	v_pk_mul_f32 v[14:15], v[14:15], v[234:235]
	v_pk_mul_f32 v[10:11], v[10:11], v[238:239]
	v_pk_mul_f32 v[6:7], v[6:7], v[242:243]
	s_waitcnt lgkmcnt(0)
	v_pk_mul_f32 v[2:3], v[2:3], v[246:247]
	v_pk_mul_f32 v[0:1], v[0:1], v[244:245]
	v_pk_mul_f32 v[44:45], v[44:45], v[232:233]
	v_pk_mul_f32 v[40:41], v[40:41], v[236:237]
	v_pk_mul_f32 v[36:37], v[36:37], v[240:241]
	v_pk_mul_f32 v[46:47], v[46:47], v[234:235]
	v_pk_mul_f32 v[42:43], v[42:43], v[238:239]
	v_pk_mul_f32 v[38:39], v[38:39], v[242:243]
	v_pk_mul_f32 v[34:35], v[34:35], v[246:247]
	v_pk_mul_f32 v[32:33], v[32:33], v[244:245]
	v_pk_mul_f32 v[28:29], v[28:29], v[232:233]
	v_pk_mul_f32 v[24:25], v[24:25], v[236:237]
	v_pk_mul_f32 v[20:21], v[20:21], v[240:241]
	v_pk_mul_f32 v[30:31], v[30:31], v[234:235]
	v_pk_mul_f32 v[26:27], v[26:27], v[238:239]
	v_pk_mul_f32 v[22:23], v[22:23], v[242:243]
	v_pk_mul_f32 v[18:19], v[18:19], v[246:247]
	v_pk_mul_f32 v[16:17], v[16:17], v[244:245]
	v_pk_mul_f32 v[60:61], v[60:61], v[232:233]
	v_pk_mul_f32 v[56:57], v[56:57], v[236:237]
	v_pk_mul_f32 v[52:53], v[52:53], v[240:241]
	v_pk_mul_f32 v[62:63], v[62:63], v[234:235]
	v_pk_mul_f32 v[58:59], v[58:59], v[238:239]
	v_pk_mul_f32 v[54:55], v[54:55], v[242:243]
	v_pk_mul_f32 v[50:51], v[50:51], v[246:247]
	v_pk_mul_f32 v[48:49], v[48:49], v[244:245]
